# final phase token loop: loads of column chunks 1..4 (ymix + 4 parameter rows each) issued at the top of the iteration with the first batch instead of one serialized load/wait stage per chunk; plus ssm
# speedup vs baseline: 1.0046x; 1.0046x over previous
; __device__ __forceinline__ float bflo(uint32_t w) { return __uint_as_float(w << 16); }
; __device__ __forceinline__ float bfhi(uint32_t w) { return __uint_as_float(w & 0xffff0000u); }
; __device__ void phase_exp_final(KParams& p, int bid, int nb, char* smem) {
;     ...
;   for (int t = bid * 4 + w; t < T; t += nb * 4) {
;     const int b = t / L;
;     float4 y[8], xo[8];
; #pragma unroll
;     for (int c = 0; c < 8; ++c) {
;       const uint2 yq = *reinterpret_cast<const uint2*>(yf + (size_t)t * D + c * 256 + lane * 4);
;       y[c] = float4{bflo(yq.x), bfhi(yq.x), bflo(yq.y), bfhi(yq.y)};
;       xo[c] = *reinterpret_cast<const float4*>(p.x + (size_t)t * D + c * 256 + lane * 4);
;     }
;     const float rmix = p.partial[t];
;     float ss = 0.f;
; #pragma unroll
;     for (int c = 0; c < 8; ++c) ss += y[c].x * y[c].x + y[c].y * y[c].y + y[c].z * y[c].z + y[c].w * y[c].w;
;     ss = wave_sum_fast(ss);
;     const float rstd = rsqrtf(ss * (1.f / D) + EPS);
;     ...
;     for (int c = 0; c < 8; ++c) {
;       const int e0 = c * 256 + lane * 4;
;       const uint2 mq = *reinterpret_cast<const uint2*>(ymix + (size_t)t * D + e0);
;       const float4 m4 = float4{bflo(mq.x), bfhi(mq.x), bflo(mq.y), bfhi(mq.y)};
;       const float4 g4 = *reinterpret_cast<const float4*>(gfx + e0), gp = *reinterpret_cast<const float4*>(p.g_post_ffn + e0);
;       const float4 h4 = *reinterpret_cast<const float4*>(gm + e0), hp = *reinterpret_cast<const float4*>(p.g_post_mix + e0);
.LBB0_1449:
	v_add_co_u32_e32 v2, vcc, 0x2000000, v60
	v_lshl_add_u64 v[0:1], v[64:65], 0, v[188:189]
	global_load_dwordx2 v[82:83], v[60:61], off
	v_addc_co_u32_e32 v3, vcc, 0, v61, vcc
	global_load_dword v80, v[58:59], off
	global_load_dwordx4 v[28:31], v[38:39], off
	global_load_dwordx4 v[112:115], v[40:41], off
	global_load_dwordx4 v[32:35], v[0:1], off
	global_load_dwordx4 v[24:27], v[0:1], off offset:1024
	global_load_dwordx4 v[20:23], v[0:1], off offset:2048
	global_load_dwordx4 v[16:19], v[0:1], off offset:3072
	global_load_dwordx2 v[92:93], v[2:3], off
	global_load_dwordx2 v[94:95], v[2:3], off offset:512
	global_load_dwordx2 v[98:99], v[2:3], off offset:1024
	global_load_dwordx2 v[100:101], v[2:3], off offset:1536
	global_load_dwordx2 v[104:105], v[2:3], off offset:2048
	global_load_dwordx2 v[124:125], v[2:3], off offset:2560
	global_load_dwordx2 v[126:127], v[2:3], off offset:3072
	global_load_dwordx2 v[128:129], v[2:3], off offset:3584
	v_ashrrev_i32_e32 v4, 31, v186
	v_lshrrev_b32_e32 v4, 21, v4
	v_add_co_u32_e32 v84, vcc, s1, v0
	v_add_u32_e32 v88, v186, v4
	s_nop 0
	v_addc_co_u32_e32 v85, vcc, 0, v1, vcc
	global_load_dwordx4 v[12:15], v[84:85], off
	global_load_dwordx4 v[8:11], v[84:85], off offset:1024
	global_load_dwordx4 v[4:7], v[84:85], off offset:2048
	global_load_dwordx4 v[0:3], v[84:85], off offset:3072
	v_ashrrev_i32_e32 v84, 11, v88
	v_mul_hi_i32_i24_e32 v85, 0xc000, v84
	v_mul_i32_i24_e32 v84, 0xc000, v84
	v_lshl_add_u64 v[84:85], s[6:7], 0, v[84:85]
	v_lshl_add_u64 v[88:89], v[84:85], 0, s[12:13]
	v_lshl_add_u64 v[90:91], v[84:85], 0, s[14:15]
	v_lshl_add_u64 v[84:85], v[88:89], 0, v[36:37]
	v_lshl_add_u64 v[102:103], v[90:91], 0, v[36:37]
	global_load_dwordx4 v[116:119], v[84:85], off
	global_load_dwordx4 v[120:123], v[102:103], off
	v_lshl_add_u64 v[86:87], v[62:63], 0, v[188:189]
	v_lshl_add_u64 v[130:131], v[88:89], 0, v[66:67]
	v_lshl_add_u64 v[132:133], v[90:91], 0, v[66:67]
	v_add_u32_e32 v186, s0, v186
	v_lshl_add_u64 v[58:59], v[58:59], 0, s[2:3]
	v_lshl_add_u64 v[62:63], v[62:63], 0, s[8:9]
	v_lshl_add_u64 v[64:65], v[64:65], 0, s[8:9]
	global_load_dwordx2 v[172:173], v[60:61], off offset:512
	global_load_dwordx4 v[192:195], v[38:39], off offset:1024
	global_load_dwordx4 v[196:199], v[40:41], off offset:1024
	global_load_dwordx4 v[200:203], v[132:133], off
	global_load_dwordx4 v[204:207], v[130:131], off
	global_load_dwordx2 v[174:175], v[60:61], off offset:1024
	global_load_dwordx4 v[208:211], v[38:39], off offset:2048
	global_load_dwordx4 v[212:215], v[40:41], off offset:2048
	global_load_dwordx4 v[216:219], v[132:133], off offset:1024
	global_load_dwordx4 v[220:223], v[130:131], off offset:1024
	global_load_dwordx2 v[176:177], v[60:61], off offset:1536
	global_load_dwordx4 v[224:227], v[38:39], off offset:3072
	global_load_dwordx4 v[228:231], v[40:41], off offset:3072
	global_load_dwordx4 v[232:235], v[132:133], off offset:2048
	global_load_dwordx4 v[236:239], v[130:131], off offset:2048
	global_load_dwordx2 v[190:191], v[60:61], off offset:2048
	global_load_dwordx4 v[240:243], v[42:43], off
	global_load_dwordx4 v[244:247], v[44:45], off
	global_load_dwordx4 v[248:251], v[132:133], off offset:3072
	global_load_dwordx4 v[252:255], v[130:131], off offset:3072
	s_waitcnt vmcnt(33)
	v_lshlrev_b32_e32 v138, 16, v92
	v_lshlrev_b32_e32 v84, 16, v82
	v_and_b32_e32 v85, 0xffff0000, v82
	v_lshlrev_b32_e32 v82, 16, v83
	v_and_b32_e32 v83, 0xffff0000, v83
	v_and_b32_e32 v139, 0xffff0000, v92
	s_waitcnt vmcnt(32)
	v_lshlrev_b32_e32 v142, 16, v94
	v_and_b32_e32 v143, 0xffff0000, v94
	v_pk_mul_f32 v[134:135], v[80:81], v[84:85] op_sel_hi:[0,1]
	v_pk_mul_f32 v[136:137], v[80:81], v[82:83] op_sel_hi:[0,1]
	v_lshlrev_b32_e32 v140, 16, v93
	v_and_b32_e32 v141, 0xffff0000, v93
	v_lshlrev_b32_e32 v144, 16, v95
	v_and_b32_e32 v145, 0xffff0000, v95
	s_waitcnt vmcnt(31)
	v_lshlrev_b32_e32 v146, 16, v98
	v_and_b32_e32 v147, 0xffff0000, v98
	v_lshlrev_b32_e32 v148, 16, v99
	v_and_b32_e32 v149, 0xffff0000, v99
	s_waitcnt vmcnt(30)
	v_lshlrev_b32_e32 v108, 16, v100
	v_and_b32_e32 v109, 0xffff0000, v100
	v_lshlrev_b32_e32 v106, 16, v101
	v_and_b32_e32 v107, 0xffff0000, v101
	s_waitcnt vmcnt(28)
	v_lshlrev_b32_e32 v100, 16, v124
	v_and_b32_e32 v101, 0xffff0000, v124
	v_lshlrev_b32_e32 v98, 16, v125
	v_and_b32_e32 v99, 0xffff0000, v125
	s_waitcnt vmcnt(26)
	v_lshlrev_b32_e32 v82, 16, v128
	v_and_b32_e32 v83, 0xffff0000, v128
	v_lshlrev_b32_e32 v84, 16, v129
	v_and_b32_e32 v85, 0xffff0000, v129
	v_pk_mul_f32 v[124:125], v[138:139], v[138:139]
	v_pk_mul_f32 v[128:129], v[142:143], v[142:143]
	v_and_b32_e32 v103, 0xffff0000, v104
	v_lshlrev_b32_e32 v94, 16, v126
	v_and_b32_e32 v95, 0xffff0000, v126
	v_lshlrev_b32_e32 v92, 16, v127
	v_and_b32_e32 v93, 0xffff0000, v127
	v_pk_mul_f32 v[112:113], v[134:135], v[112:113]
	v_pk_mul_f32 v[114:115], v[136:137], v[114:115]
	v_pk_mul_f32 v[126:127], v[140:141], v[140:141]
	v_pk_mul_f32 v[134:135], v[144:145], v[144:145]
	v_pk_mul_f32 v[136:137], v[146:147], v[146:147]
	v_add_f32_e32 v96, v128, v129
	v_add_f32_e32 v111, v124, v125
	v_lshlrev_b32_e32 v102, 16, v104
	v_pk_mul_f32 v[150:151], v[148:149], v[148:149]
	v_pk_mul_f32 v[152:153], v[108:109], v[108:109]
	v_mov_b32_e32 v158, v103
	v_mov_b32_e32 v159, v101
	v_add_f32_e32 v136, v136, v137
	v_add_f32_e32 v96, v96, v134
	v_add_f32_e32 v111, v111, v126
	v_lshlrev_b32_e32 v104, 16, v105
	v_pk_mul_f32 v[154:155], v[106:107], v[106:107]
	v_mov_b32_e32 v156, v102
	v_mov_b32_e32 v157, v100
	v_pk_mul_f32 v[158:159], v[158:159], v[158:159]
	v_add_f32_e32 v137, v152, v153
	v_add_f32_e32 v126, v136, v150
	v_add_f32_e32 v96, v135, v96
	v_add_f32_e32 v111, v127, v111
	v_and_b32_e32 v105, 0xffff0000, v105
	v_mov_b32_e32 v160, v104
	v_mov_b32_e32 v161, v98
	v_mov_b32_e32 v166, v95
	v_mov_b32_e32 v167, v83
	v_pk_fma_f32 v[124:125], v[156:157], v[156:157], v[158:159]
	v_add_f32_e32 v134, v137, v154
	v_add_f32_e32 v135, v151, v126
	v_add_f32_e32 v96, v111, v96
	v_mov_b32_e32 v162, v105
	v_mov_b32_e32 v163, v99
	v_mov_b32_e32 v164, v94
	v_mov_b32_e32 v165, v82
	v_pk_mul_f32 v[166:167], v[166:167], v[166:167]
	v_pk_fma_f32 v[124:125], v[160:161], v[160:161], v[124:125]
	v_add_f32_e32 v134, v155, v134
	v_add_f32_e32 v96, v96, v135
	v_mov_b32_e32 v168, v92
	v_mov_b32_e32 v169, v84
	v_pk_fma_f32 v[128:129], v[164:165], v[164:165], v[166:167]
	v_pk_fma_f32 v[124:125], v[162:163], v[162:163], v[124:125]
	v_add_f32_e32 v96, v96, v134
	v_mov_b32_e32 v170, v93
	v_mov_b32_e32 v171, v85
	v_pk_fma_f32 v[128:129], v[168:169], v[168:169], v[128:129]
	v_add_f32_e32 v96, v96, v124
	v_pk_fma_f32 v[126:127], v[170:171], v[170:171], v[128:129]
	v_add_f32_e32 v96, v96, v125
	v_add_f32_e32 v96, v96, v126
	v_add_f32_e32 v96, v96, v127
	s_waitcnt vmcnt(20)
; __device__ __forceinline__ float bflo(uint32_t w) { return __uint_as_float(w << 16); }
; __device__ __forceinline__ float bfhi(uint32_t w) { return __uint_as_float(w & 0xffff0000u); }
; __device__ void phase_exp_final(KParams& p, int bid, int nb, char* smem) {
;     ...
;     ss = wave_sum_fast(ss);
;     const float rstd = rsqrtf(ss * (1.f / D) + EPS);
;     const float* gfx = p.mod + (size_t)b * NMOD + 5 * D;
;     const float* gm = p.mod + (size_t)b * NMOD + 2 * D;
; #pragma unroll
;     for (int c = 0; c < 8; ++c) {
;       const int e0 = c * 256 + lane * 4;
;       const uint2 mq = *reinterpret_cast<const uint2*>(ymix + (size_t)t * D + e0);
;       const float4 m4 = float4{bflo(mq.x), bfhi(mq.x), bflo(mq.y), bfhi(mq.y)};
;       const float4 g4 = *reinterpret_cast<const float4*>(gfx + e0), gp = *reinterpret_cast<const float4*>(p.g_post_ffn + e0);
;       const float4 h4 = *reinterpret_cast<const float4*>(gm + e0), hp = *reinterpret_cast<const float4*>(p.g_post_mix + e0);
;       xo[c].x += h4.x * (m4.x * rmix * hp.x) + g4.x * (y[c].x * rstd * gp.x);
;       xo[c].y += h4.y * (m4.y * rmix * hp.y) + g4.y * (y[c].y * rstd * gp.y);
;       xo[c].z += h4.z * (m4.z * rmix * hp.z) + g4.z * (y[c].z * rstd * gp.z);
;       xo[c].w += h4.w * (m4.w * rmix * hp.w) + g4.w * (y[c].w * rstd * gp.w);
;       *reinterpret_cast<float4*>(p.out + (size_t)t * D + e0) = xo[c];
	v_pk_mul_f32 v[112:113], v[120:121], v[112:113]
	v_pk_mul_f32 v[114:115], v[122:123], v[114:115]
	v_add_f32_dpp v96, v96, v96 quad_perm:[1,0,3,2] row_mask:0xf bank_mask:0xf bound_ctrl:1
	v_lshl_add_u64 v[124:125], v[90:91], 0, v[68:69]
	s_nop 0
	v_add_f32_dpp v96, v96, v96 quad_perm:[2,3,0,1] row_mask:0xf bank_mask:0xf bound_ctrl:1
	s_nop 1
	v_add_f32_dpp v96, v96, v96 row_ror:4 row_mask:0xf bank_mask:0xf bound_ctrl:1
	s_nop 1
	v_add_f32_dpp v96, v96, v96 row_ror:8 row_mask:0xf bank_mask:0xf bound_ctrl:1
	ds_bpermute_b32 v111, v81, v96
	s_waitcnt lgkmcnt(0)
	v_add_f32_e32 v96, v96, v111
	ds_bpermute_b32 v111, v97, v96
	s_waitcnt lgkmcnt(0)
	v_add_f32_e32 v96, v96, v111
	v_fmamk_f32 v96, v96, 0x3a000000, v110
	v_mul_f32_e32 v111, 0x4b800000, v96
	v_cmp_gt_f32_e32 vcc, s16, v96
	s_nop 1
	v_cndmask_b32_e32 v96, v96, v111, vcc
	v_rsq_f32_e32 v96, v96
	s_nop 0
	v_mul_f32_e32 v111, 0x45800000, v96
	v_cndmask_b32_e32 v96, v96, v111, vcc
	v_pk_mul_f32 v[120:121], v[96:97], v[138:139] op_sel_hi:[0,1]
	v_pk_mul_f32 v[122:123], v[96:97], v[140:141] op_sel_hi:[0,1]
	v_pk_mul_f32 v[28:29], v[28:29], v[120:121]
	v_pk_mul_f32 v[30:31], v[30:31], v[122:123]
	v_pk_fma_f32 v[28:29], v[116:117], v[28:29], v[112:113]
	v_pk_fma_f32 v[30:31], v[118:119], v[30:31], v[114:115]
	v_pk_add_f32 v[28:29], v[32:33], v[28:29]
	v_pk_add_f32 v[30:31], v[34:35], v[30:31]
	global_store_dwordx4 v[86:87], v[28:31], off
	s_waitcnt vmcnt(16)
	v_mov_b32_e32 v120, v172
	v_mov_b32_e32 v121, v173
	s_nop 0
	v_mov_b32_e32 v28, v192
	v_mov_b32_e32 v29, v193
	v_mov_b32_e32 v30, v194
	v_mov_b32_e32 v31, v195
	v_mov_b32_e32 v32, v196
	v_mov_b32_e32 v33, v197
	v_mov_b32_e32 v34, v198
	v_mov_b32_e32 v35, v199
	v_mov_b32_e32 v112, v200
	v_mov_b32_e32 v113, v201
	v_mov_b32_e32 v114, v202
	v_mov_b32_e32 v115, v203
	v_mov_b32_e32 v116, v204
	v_mov_b32_e32 v117, v205
	v_mov_b32_e32 v118, v206
	v_mov_b32_e32 v119, v207
	v_pk_mul_f32 v[126:127], v[96:97], v[142:143] op_sel_hi:[0,1]
	v_pk_mul_f32 v[128:129], v[96:97], v[144:145] op_sel_hi:[0,1]
	v_lshl_add_u64 v[122:123], v[88:89], 0, v[68:69]
	v_pk_mul_f32 v[108:109], v[96:97], v[108:109] op_sel_hi:[0,1]
	v_pk_mul_f32 v[106:107], v[96:97], v[106:107] op_sel_hi:[0,1]
	v_pk_mul_f32 v[102:103], v[96:97], v[102:103] op_sel_hi:[0,1]
	v_pk_mul_f32 v[104:105], v[96:97], v[104:105] op_sel_hi:[0,1]
	v_pk_mul_f32 v[98:99], v[96:97], v[98:99] op_sel_hi:[0,1]
	v_lshlrev_b32_e32 v130, 16, v120
	v_and_b32_e32 v131, 0xffff0000, v120
	v_lshlrev_b32_e32 v120, 16, v121
	v_and_b32_e32 v121, 0xffff0000, v121
	v_pk_mul_f32 v[28:29], v[126:127], v[28:29]
	v_pk_mul_f32 v[126:127], v[80:81], v[130:131] op_sel_hi:[0,1]
	v_pk_mul_f32 v[120:121], v[80:81], v[120:121] op_sel_hi:[0,1]
	v_pk_mul_f32 v[32:33], v[126:127], v[32:33]
	v_pk_mul_f32 v[34:35], v[120:121], v[34:35]
	v_pk_mul_f32 v[30:31], v[128:129], v[30:31]
	v_pk_mul_f32 v[32:33], v[112:113], v[32:33]
	v_pk_mul_f32 v[34:35], v[114:115], v[34:35]
	v_pk_fma_f32 v[28:29], v[116:117], v[28:29], v[32:33]
	v_pk_fma_f32 v[30:31], v[118:119], v[30:31], v[34:35]
	v_pk_add_f32 v[24:25], v[24:25], v[28:29]
	v_pk_add_f32 v[26:27], v[26:27], v[30:31]
	global_store_dwordx4 v[86:87], v[24:27], off offset:1024
	s_waitcnt vmcnt(12)
	v_mov_b32_e32 v116, v174
	v_mov_b32_e32 v117, v175
	s_nop 0
	v_mov_b32_e32 v24, v208
	v_mov_b32_e32 v25, v209
	v_mov_b32_e32 v26, v210
	v_mov_b32_e32 v27, v211
	v_mov_b32_e32 v28, v212
	v_mov_b32_e32 v29, v213
	v_mov_b32_e32 v30, v214
	v_mov_b32_e32 v31, v215
	v_mov_b32_e32 v32, v216
	v_mov_b32_e32 v33, v217
	v_mov_b32_e32 v34, v218
	v_mov_b32_e32 v35, v219
	v_mov_b32_e32 v112, v220
	v_mov_b32_e32 v113, v221
	v_mov_b32_e32 v114, v222
	v_mov_b32_e32 v115, v223
	v_pk_mul_f32 v[122:123], v[96:97], v[146:147] op_sel_hi:[0,1]
	v_pk_mul_f32 v[124:125], v[96:97], v[148:149] op_sel_hi:[0,1]
	v_lshl_add_u64 v[118:119], v[88:89], 0, v[70:71]
	v_lshl_add_u64 v[120:121], v[90:91], 0, v[70:71]
	v_lshlrev_b32_e32 v126, 16, v116
	v_and_b32_e32 v127, 0xffff0000, v116
	v_lshlrev_b32_e32 v116, 16, v117
	v_and_b32_e32 v117, 0xffff0000, v117
	v_pk_mul_f32 v[24:25], v[122:123], v[24:25]
	v_pk_mul_f32 v[122:123], v[80:81], v[126:127] op_sel_hi:[0,1]
	v_pk_mul_f32 v[116:117], v[80:81], v[116:117] op_sel_hi:[0,1]
	v_pk_mul_f32 v[28:29], v[122:123], v[28:29]
	v_pk_mul_f32 v[30:31], v[116:117], v[30:31]
	v_pk_mul_f32 v[26:27], v[124:125], v[26:27]
	v_pk_mul_f32 v[28:29], v[32:33], v[28:29]
	v_pk_mul_f32 v[30:31], v[34:35], v[30:31]
	v_pk_fma_f32 v[24:25], v[112:113], v[24:25], v[28:29]
	v_pk_fma_f32 v[26:27], v[114:115], v[26:27], v[30:31]
	v_pk_add_f32 v[20:21], v[20:21], v[24:25]
	v_pk_add_f32 v[22:23], v[22:23], v[26:27]
	global_store_dwordx4 v[86:87], v[20:23], off offset:2048
	s_waitcnt vmcnt(8)
	v_mov_b32_e32 v112, v176
	v_mov_b32_e32 v113, v177
	s_nop 0
	v_mov_b32_e32 v20, v224
	v_mov_b32_e32 v21, v225
	v_mov_b32_e32 v22, v226
	v_mov_b32_e32 v23, v227
	v_mov_b32_e32 v24, v228
	v_mov_b32_e32 v25, v229
	v_mov_b32_e32 v26, v230
	v_mov_b32_e32 v27, v231
	v_mov_b32_e32 v28, v232
	v_mov_b32_e32 v29, v233
	v_mov_b32_e32 v30, v234
	v_mov_b32_e32 v31, v235
	v_mov_b32_e32 v32, v236
	v_mov_b32_e32 v33, v237
	v_mov_b32_e32 v34, v238
	v_mov_b32_e32 v35, v239
	v_lshl_add_u64 v[114:115], v[88:89], 0, v[72:73]
	v_lshl_add_u64 v[116:117], v[90:91], 0, v[72:73]
	v_lshlrev_b32_e32 v118, 16, v112
	v_and_b32_e32 v119, 0xffff0000, v112
	v_lshlrev_b32_e32 v112, 16, v113
	v_and_b32_e32 v113, 0xffff0000, v113
	v_pk_mul_f32 v[20:21], v[108:109], v[20:21]
	v_pk_mul_f32 v[22:23], v[106:107], v[22:23]
	v_pk_mul_f32 v[106:107], v[80:81], v[118:119] op_sel_hi:[0,1]
	v_pk_mul_f32 v[108:109], v[80:81], v[112:113] op_sel_hi:[0,1]
	v_pk_mul_f32 v[24:25], v[106:107], v[24:25]
	v_pk_mul_f32 v[26:27], v[108:109], v[26:27]
	v_pk_mul_f32 v[24:25], v[28:29], v[24:25]
	v_pk_mul_f32 v[26:27], v[30:31], v[26:27]
	v_pk_fma_f32 v[20:21], v[32:33], v[20:21], v[24:25]
	v_pk_fma_f32 v[22:23], v[34:35], v[22:23], v[26:27]
	v_pk_add_f32 v[16:17], v[16:17], v[20:21]
	v_pk_add_f32 v[18:19], v[18:19], v[22:23]
	global_store_dwordx4 v[86:87], v[16:19], off offset:3072
	s_waitcnt vmcnt(4)
; __device__ __forceinline__ float bflo(uint32_t w) { return __uint_as_float(w << 16); }
; __device__ __forceinline__ float bfhi(uint32_t w) { return __uint_as_float(w & 0xffff0000u); }
; __device__ void phase_exp_final(KParams& p, int bid, int nb, char* smem) {
;     ...
; #pragma unroll
;     for (int c = 0; c < 8; ++c) {
;       const int e0 = c * 256 + lane * 4;
;       const uint2 mq = *reinterpret_cast<const uint2*>(ymix + (size_t)t * D + e0);
;       const float4 m4 = float4{bflo(mq.x), bfhi(mq.x), bflo(mq.y), bfhi(mq.y)};
;       const float4 g4 = *reinterpret_cast<const float4*>(gfx + e0), gp = *reinterpret_cast<const float4*>(p.g_post_ffn + e0);
;       const float4 h4 = *reinterpret_cast<const float4*>(gm + e0), hp = *reinterpret_cast<const float4*>(p.g_post_mix + e0);
;       xo[c].x += h4.x * (m4.x * rmix * hp.x) + g4.x * (y[c].x * rstd * gp.x);
;       xo[c].y += h4.y * (m4.y * rmix * hp.y) + g4.y * (y[c].y * rstd * gp.y);
;       xo[c].z += h4.z * (m4.z * rmix * hp.z) + g4.z * (y[c].z * rstd * gp.z);
;       xo[c].w += h4.w * (m4.w * rmix * hp.w) + g4.w * (y[c].w * rstd * gp.w);
;       *reinterpret_cast<float4*>(p.out + (size_t)t * D + e0) = xo[c];
;     }
	v_mov_b32_e32 v32, v190
	v_mov_b32_e32 v33, v191
	s_nop 0
	v_mov_b32_e32 v16, v240
	v_mov_b32_e32 v17, v241
	v_mov_b32_e32 v18, v242
	v_mov_b32_e32 v19, v243
	v_mov_b32_e32 v20, v244
	v_mov_b32_e32 v21, v245
	v_mov_b32_e32 v22, v246
	v_mov_b32_e32 v23, v247
	v_mov_b32_e32 v24, v248
	v_mov_b32_e32 v25, v249
	v_mov_b32_e32 v26, v250
	v_mov_b32_e32 v27, v251
	v_mov_b32_e32 v28, v252
	v_mov_b32_e32 v29, v253
	v_mov_b32_e32 v30, v254
	v_mov_b32_e32 v31, v255
	v_add_co_u32_e32 v34, vcc, s1, v86
	v_lshl_add_u64 v[106:107], v[90:91], 0, v[74:75]
	s_nop 0
	v_addc_co_u32_e32 v35, vcc, 0, v87, vcc
	v_lshl_add_u64 v[86:87], v[88:89], 0, v[74:75]
	v_cmp_lt_i32_e32 vcc, s17, v186
	s_or_b64 s[10:11], vcc, s[10:11]
	v_lshlrev_b32_e32 v108, 16, v32
	v_and_b32_e32 v109, 0xffff0000, v32
	v_lshlrev_b32_e32 v32, 16, v33
	v_and_b32_e32 v33, 0xffff0000, v33
	v_pk_mul_f32 v[16:17], v[102:103], v[16:17]
	v_pk_mul_f32 v[102:103], v[80:81], v[108:109] op_sel_hi:[0,1]
	v_pk_mul_f32 v[32:33], v[80:81], v[32:33] op_sel_hi:[0,1]
	v_pk_mul_f32 v[20:21], v[102:103], v[20:21]
	v_pk_mul_f32 v[22:23], v[32:33], v[22:23]
	v_pk_mul_f32 v[18:19], v[104:105], v[18:19]
	v_pk_mul_f32 v[20:21], v[24:25], v[20:21]
	v_pk_mul_f32 v[22:23], v[26:27], v[22:23]
	v_pk_fma_f32 v[16:17], v[28:29], v[16:17], v[20:21]
	v_pk_fma_f32 v[18:19], v[30:31], v[18:19], v[22:23]
	v_pk_add_f32 v[12:13], v[12:13], v[16:17]
	v_pk_add_f32 v[14:15], v[14:15], v[18:19]
	global_store_dwordx4 v[34:35], v[12:15], off
	global_load_dwordx2 v[28:29], v[60:61], off offset:2560
	s_nop 0
	global_load_dwordx4 v[12:15], v[46:47], off
	global_load_dwordx4 v[16:19], v[48:49], off
	global_load_dwordx4 v[20:23], v[106:107], off
	global_load_dwordx4 v[24:27], v[86:87], off
	v_pk_mul_f32 v[86:87], v[96:97], v[100:101] op_sel_hi:[0,1]
	v_lshl_add_u64 v[30:31], v[88:89], 0, v[76:77]
	v_lshl_add_u64 v[32:33], v[90:91], 0, v[76:77]
	s_waitcnt vmcnt(4)
	v_lshlrev_b32_e32 v100, 16, v28
	v_and_b32_e32 v101, 0xffff0000, v28
	v_lshlrev_b32_e32 v28, 16, v29
	v_and_b32_e32 v29, 0xffff0000, v29
	s_waitcnt vmcnt(3)
	v_pk_mul_f32 v[12:13], v[86:87], v[12:13]
	v_pk_mul_f32 v[86:87], v[80:81], v[100:101] op_sel_hi:[0,1]
	v_pk_mul_f32 v[28:29], v[80:81], v[28:29] op_sel_hi:[0,1]
	s_waitcnt vmcnt(2)
	v_pk_mul_f32 v[16:17], v[86:87], v[16:17]
	v_pk_mul_f32 v[18:19], v[28:29], v[18:19]
	v_pk_mul_f32 v[14:15], v[98:99], v[14:15]
	s_waitcnt vmcnt(1)
	v_pk_mul_f32 v[16:17], v[20:21], v[16:17]
	v_pk_mul_f32 v[18:19], v[22:23], v[18:19]
	s_waitcnt vmcnt(0)
	v_pk_fma_f32 v[12:13], v[24:25], v[12:13], v[16:17]
	v_pk_fma_f32 v[14:15], v[26:27], v[14:15], v[18:19]
	v_pk_add_f32 v[8:9], v[8:9], v[12:13]
	v_pk_add_f32 v[10:11], v[10:11], v[14:15]
	global_store_dwordx4 v[34:35], v[8:11], off offset:1024
	global_load_dwordx2 v[24:25], v[60:61], off offset:3072
	s_nop 0
	global_load_dwordx4 v[8:11], v[50:51], off
	global_load_dwordx4 v[12:15], v[52:53], off
	global_load_dwordx4 v[16:19], v[32:33], off
	global_load_dwordx4 v[20:23], v[30:31], off
	v_pk_mul_f32 v[30:31], v[96:97], v[94:95] op_sel_hi:[0,1]
	v_pk_mul_f32 v[32:33], v[96:97], v[92:93] op_sel_hi:[0,1]
	v_lshl_add_u64 v[26:27], v[88:89], 0, v[78:79]
	v_lshl_add_u64 v[28:29], v[90:91], 0, v[78:79]
	s_waitcnt vmcnt(4)
	v_lshlrev_b32_e32 v86, 16, v24
	v_and_b32_e32 v87, 0xffff0000, v24
	v_lshlrev_b32_e32 v24, 16, v25
	v_and_b32_e32 v25, 0xffff0000, v25
	s_waitcnt vmcnt(3)
	v_pk_mul_f32 v[8:9], v[30:31], v[8:9]
	v_pk_mul_f32 v[30:31], v[80:81], v[86:87] op_sel_hi:[0,1]
	v_pk_mul_f32 v[24:25], v[80:81], v[24:25] op_sel_hi:[0,1]
	s_waitcnt vmcnt(2)
	v_pk_mul_f32 v[12:13], v[30:31], v[12:13]
	v_pk_mul_f32 v[14:15], v[24:25], v[14:15]
	v_pk_mul_f32 v[10:11], v[32:33], v[10:11]
	s_waitcnt vmcnt(1)
	v_pk_mul_f32 v[12:13], v[16:17], v[12:13]
	v_pk_mul_f32 v[14:15], v[18:19], v[14:15]
	s_waitcnt vmcnt(0)
	v_pk_fma_f32 v[8:9], v[20:21], v[8:9], v[12:13]
	v_pk_fma_f32 v[10:11], v[22:23], v[10:11], v[14:15]
	v_pk_add_f32 v[4:5], v[4:5], v[8:9]
	v_pk_add_f32 v[6:7], v[6:7], v[10:11]
	global_store_dwordx4 v[34:35], v[4:7], off offset:2048
	global_load_dwordx2 v[20:21], v[60:61], off offset:3584
	s_nop 0
	global_load_dwordx4 v[4:7], v[54:55], off
	global_load_dwordx4 v[8:11], v[56:57], off
	global_load_dwordx4 v[12:15], v[28:29], off
	global_load_dwordx4 v[16:19], v[26:27], off
	v_pk_mul_f32 v[22:23], v[96:97], v[82:83] op_sel_hi:[0,1]
	v_pk_mul_f32 v[24:25], v[96:97], v[84:85] op_sel_hi:[0,1]
	v_lshl_add_u64 v[60:61], v[60:61], 0, s[4:5]
	s_waitcnt vmcnt(4)
	v_lshlrev_b32_e32 v26, 16, v20
	v_and_b32_e32 v27, 0xffff0000, v20
	v_lshlrev_b32_e32 v20, 16, v21
	v_and_b32_e32 v21, 0xffff0000, v21
	s_waitcnt vmcnt(3)
	v_pk_mul_f32 v[4:5], v[22:23], v[4:5]
	v_pk_mul_f32 v[22:23], v[80:81], v[26:27] op_sel_hi:[0,1]
	v_pk_mul_f32 v[20:21], v[80:81], v[20:21] op_sel_hi:[0,1]
	s_waitcnt vmcnt(2)
	v_pk_mul_f32 v[8:9], v[22:23], v[8:9]
	v_pk_mul_f32 v[10:11], v[20:21], v[10:11]
	v_pk_mul_f32 v[6:7], v[24:25], v[6:7]
	s_waitcnt vmcnt(1)
	v_pk_mul_f32 v[8:9], v[12:13], v[8:9]
	v_pk_mul_f32 v[10:11], v[14:15], v[10:11]
	s_waitcnt vmcnt(0)
	v_pk_fma_f32 v[4:5], v[16:17], v[4:5], v[8:9]
	v_pk_fma_f32 v[6:7], v[18:19], v[6:7], v[10:11]
	v_pk_add_f32 v[0:1], v[0:1], v[4:5]
	v_pk_add_f32 v[2:3], v[2:3], v[6:7]
	global_store_dwordx4 v[34:35], v[0:3], off offset:3072
	s_andn2_b64 exec, exec, s[10:11]
	s_cbranch_execnz .LBB0_1449

; __global__ void __launch_bounds__(NTHREADS, 2) fwd_mega(Params p_unused) {
	.amdhsa_kernel _ZN12_GLOBAL__N_18fwd_megaENS_6ParamsE
		.amdhsa_group_segment_fixed_size 75808
		.amdhsa_private_segment_fixed_size 0
		.amdhsa_kernarg_size 856
		.amdhsa_user_sgpr_count 2
		.amdhsa_user_sgpr_dispatch_ptr 0
		.amdhsa_user_sgpr_queue_ptr 0
		.amdhsa_user_sgpr_kernarg_segment_ptr 1
		.amdhsa_user_sgpr_dispatch_id 0
		.amdhsa_user_sgpr_kernarg_preload_length 0
		.amdhsa_user_sgpr_kernarg_preload_offset 0
		.amdhsa_user_sgpr_private_segment_size 0
		.amdhsa_uses_dynamic_stack 0
		.amdhsa_enable_private_segment 0
		.amdhsa_system_sgpr_workgroup_id_x 1
		.amdhsa_system_sgpr_workgroup_id_y 0
		.amdhsa_system_sgpr_workgroup_id_z 0
		.amdhsa_system_sgpr_workgroup_info 0
		.amdhsa_system_vgpr_workitem_id 0
		.amdhsa_next_free_vgpr 256
		.amdhsa_next_free_sgpr 102
		.amdhsa_accum_offset 256
		.amdhsa_reserve_vcc 1
		.amdhsa_float_round_mode_32 0
		.amdhsa_float_round_mode_16_64 0
		.amdhsa_float_denorm_mode_32 3
		.amdhsa_float_denorm_mode_16_64 3
		.amdhsa_dx10_clamp 1
		.amdhsa_ieee_mode 1
		.amdhsa_fp16_overflow 0
		.amdhsa_tg_split 0
		.amdhsa_exception_fp_ieee_invalid_op 0
		.amdhsa_exception_fp_denorm_src 0
		.amdhsa_exception_fp_ieee_div_zero 0
		.amdhsa_exception_fp_ieee_overflow 0
		.amdhsa_exception_fp_ieee_underflow 0
		.amdhsa_exception_fp_ieee_inexact 0
		.amdhsa_exception_int_div_zero 0
	.end_amdhsa_kernel

; __global__ void __launch_bounds__(NTHREADS, 2) fwd_mega(Params p_unused) {
amdhsa.kernels:
  - .agpr_count:     0
    .args:
      - .offset:         0
        .size:           600
        .value_kind:     by_value
      - .offset:         600
        .size:           4
        .value_kind:     hidden_block_count_x
      - .offset:         604
        .size:           4
        .value_kind:     hidden_block_count_y
      - .offset:         608
        .size:           4
        .value_kind:     hidden_block_count_z
      - .offset:         612
        .size:           2
        .value_kind:     hidden_group_size_x
      - .offset:         614
        .size:           2
        .value_kind:     hidden_group_size_y
      - .offset:         616
        .size:           2
        .value_kind:     hidden_group_size_z
      - .offset:         618
        .size:           2
        .value_kind:     hidden_remainder_x
      - .offset:         620
        .size:           2
        .value_kind:     hidden_remainder_y
      - .offset:         622
        .size:           2
        .value_kind:     hidden_remainder_z
      - .offset:         640
        .size:           8
        .value_kind:     hidden_global_offset_x
      - .offset:         648
        .size:           8
        .value_kind:     hidden_global_offset_y
      - .offset:         656
        .size:           8
        .value_kind:     hidden_global_offset_z
      - .offset:         664
        .size:           2
        .value_kind:     hidden_grid_dims
    .group_segment_fixed_size: 75808
    .kernarg_segment_align: 8
    .kernarg_segment_size: 856
    .language:       OpenCL C
    .language_version:
      - 2
      - 0
    .max_flat_workgroup_size: 256
    .name:           _ZN12_GLOBAL__N_18fwd_megaENS_6ParamsE
    .private_segment_fixed_size: 0
    .sgpr_count:     108
    .sgpr_spill_count: 4
    .symbol:         _ZN12_GLOBAL__N_18fwd_megaENS_6ParamsE.kd
    .uniform_work_group_size: 1
    .uses_dynamic_stack: false
    .vgpr_count:     256
    .vgpr_spill_count: 0
    .wavefront_size: 64
